# top-k gt emission batched 4 sites at a time (4 compares, 4 lane ranks, 4 addresses back to back; LDS writes under s_mov exec) instead of a saveexec/branch chain per site
# speedup vs baseline: 1.0016x; 1.0016x over previous
.LBB0_1259:
	s_nop 0
	s_nop 0
	s_nop 0
	s_nop 0
	s_nop 0
	s_nop 0
	s_nop 0
	s_nop 0
	s_nop 0
	s_nop 0
	s_nop 0
	s_nop 0
	s_nop 0
	s_nop 0
	s_nop 0
	s_nop 0
	s_nop 0
	s_nop 0
	s_nop 0
	s_nop 0
	s_nop 0
	s_nop 0
	s_nop 0
	s_nop 0
	s_nop 0
	s_nop 0
	s_nop 0
	s_nop 0
	s_nop 0
	s_nop 0
	s_nop 0
	s_nop 0
	s_nop 0
	s_nop 0
	s_nop 0
	s_nop 0
	s_nop 0
	s_nop 0
	s_nop 0
	s_nop 0
	s_nop 0
	s_nop 0
	s_nop 0
	s_nop 0
	s_nop 0
	s_nop 0
	s_nop 0
	s_nop 0
	s_nop 0
	s_nop 0
	s_nop 0
	s_nop 0
	s_nop 0
	s_nop 0
	s_nop 0
	s_nop 0
	s_cmp_gt_i32 s14, 0
	s_cselect_b64 s[42:43], -1, 0
	s_cmp_lt_i32 s14, 1
	s_mov_b32 s4, 0
	s_cbranch_scc1 .LBB0_1277
	s_mov_b64 s[34:35], exec
	v_cmp_gt_u32_sdwa s[70:71], v50, v66 src0_sel:WORD_0 src1_sel:DWORD
	v_cmp_gt_u32_sdwa s[88:89], v50, v66 src0_sel:WORD_1 src1_sel:DWORD
	v_cmp_gt_u32_sdwa s[90:91], v51, v66 src0_sel:WORD_0 src1_sel:DWORD
	v_cmp_gt_u32_sdwa s[94:95], v51, v66 src0_sel:WORD_1 src1_sel:DWORD
	s_lshl1_add_u32 s32, s4, s52
	v_mbcnt_lo_u32_b32 v67, s70, 0
	v_mbcnt_lo_u32_b32 v68, s88, 0
	v_mbcnt_lo_u32_b32 v69, s90, 0
	v_mbcnt_lo_u32_b32 v70, s94, 0
	s_bcnt1_i32_b64 s93, s[70:71]
	s_add_i32 s4, s4, s93
	s_lshl1_add_u32 s85, s4, s52
	v_mbcnt_hi_u32_b32 v67, s71, v67
	s_bcnt1_i32_b64 s93, s[88:89]
	s_add_i32 s4, s4, s93
	s_lshl1_add_u32 s86, s4, s52
	v_mbcnt_hi_u32_b32 v68, s89, v68
	s_bcnt1_i32_b64 s93, s[90:91]
	s_add_i32 s4, s4, s93
	s_lshl1_add_u32 s15, s4, s52
	v_mbcnt_hi_u32_b32 v69, s91, v69
	s_bcnt1_i32_b64 s93, s[94:95]
	s_add_i32 s4, s4, s93
	v_mbcnt_hi_u32_b32 v70, s95, v70
	v_lshl_add_u32 v67, v67, 1, s32
	v_lshl_add_u32 v68, v68, 1, s85
	v_lshl_add_u32 v69, v69, 1, s86
	v_lshl_add_u32 v70, v70, 1, s15
	s_mov_b64 exec, s[70:71]
	ds_write_b16 v67, v119 offset:32768
	s_mov_b64 exec, s[88:89]
	ds_write_b16 v68, v120 offset:32768
	s_mov_b64 exec, s[90:91]
	ds_write_b16 v69, v121 offset:32768
	s_mov_b64 exec, s[94:95]
	ds_write_b16 v70, v122 offset:32768
	s_mov_b64 exec, s[34:35]
	s_mov_b64 s[34:35], exec
	v_cmp_gt_u32_sdwa s[70:71], v52, v66 src0_sel:WORD_0 src1_sel:DWORD
	v_cmp_gt_u32_sdwa s[88:89], v52, v66 src0_sel:WORD_1 src1_sel:DWORD
	v_cmp_gt_u32_sdwa s[90:91], v53, v66 src0_sel:WORD_0 src1_sel:DWORD
	v_cmp_gt_u32_sdwa s[94:95], v53, v66 src0_sel:WORD_1 src1_sel:DWORD
	s_lshl1_add_u32 s32, s4, s52
	v_mbcnt_lo_u32_b32 v67, s70, 0
	v_mbcnt_lo_u32_b32 v68, s88, 0
	v_mbcnt_lo_u32_b32 v69, s90, 0
	v_mbcnt_lo_u32_b32 v70, s94, 0
	s_bcnt1_i32_b64 s93, s[70:71]
	s_add_i32 s4, s4, s93
	s_lshl1_add_u32 s85, s4, s52
	v_mbcnt_hi_u32_b32 v67, s71, v67
	s_bcnt1_i32_b64 s93, s[88:89]
	s_add_i32 s4, s4, s93
	s_lshl1_add_u32 s86, s4, s52
	v_mbcnt_hi_u32_b32 v68, s89, v68
	s_bcnt1_i32_b64 s93, s[90:91]
	s_add_i32 s4, s4, s93
	s_lshl1_add_u32 s15, s4, s52
	v_mbcnt_hi_u32_b32 v69, s91, v69
	s_bcnt1_i32_b64 s93, s[94:95]
	s_add_i32 s4, s4, s93
	v_mbcnt_hi_u32_b32 v70, s95, v70
	v_lshl_add_u32 v67, v67, 1, s32
	v_lshl_add_u32 v68, v68, 1, s85
	v_lshl_add_u32 v69, v69, 1, s86
	v_lshl_add_u32 v70, v70, 1, s15
	s_mov_b64 exec, s[70:71]
	ds_write_b16 v67, v123 offset:32768
	s_mov_b64 exec, s[88:89]
	ds_write_b16 v68, v124 offset:32768
	s_mov_b64 exec, s[90:91]
	ds_write_b16 v69, v125 offset:32768
	s_mov_b64 exec, s[94:95]
	ds_write_b16 v70, v126 offset:32768
	s_mov_b64 exec, s[34:35]

.LBB0_1292:
	s_mov_b64 s[34:35], exec
	v_cmp_gt_u32_sdwa s[70:71], v38, v66 src0_sel:WORD_0 src1_sel:DWORD
	v_cmp_gt_u32_sdwa s[88:89], v38, v66 src0_sel:WORD_1 src1_sel:DWORD
	v_cmp_gt_u32_sdwa s[90:91], v39, v66 src0_sel:WORD_0 src1_sel:DWORD
	v_cmp_gt_u32_sdwa s[94:95], v39, v66 src0_sel:WORD_1 src1_sel:DWORD
	s_lshl1_add_u32 s32, s4, s52
	v_mbcnt_lo_u32_b32 v67, s70, 0
	v_mbcnt_lo_u32_b32 v68, s88, 0
	v_mbcnt_lo_u32_b32 v69, s90, 0
	v_mbcnt_lo_u32_b32 v70, s94, 0
	s_bcnt1_i32_b64 s93, s[70:71]
	s_add_i32 s4, s4, s93
	s_lshl1_add_u32 s85, s4, s52
	v_mbcnt_hi_u32_b32 v67, s71, v67
	s_bcnt1_i32_b64 s93, s[88:89]
	s_add_i32 s4, s4, s93
	s_lshl1_add_u32 s86, s4, s52
	v_mbcnt_hi_u32_b32 v68, s89, v68
	s_bcnt1_i32_b64 s93, s[90:91]
	s_add_i32 s4, s4, s93
	s_lshl1_add_u32 s15, s4, s52
	v_mbcnt_hi_u32_b32 v69, s91, v69
	s_bcnt1_i32_b64 s93, s[94:95]
	s_add_i32 s4, s4, s93
	v_mbcnt_hi_u32_b32 v70, s95, v70
	v_or_b32_e32 v71, 0x200, v119
	v_or_b32_e32 v72, 0x201, v119
	v_or_b32_e32 v73, 0x202, v119
	v_or_b32_e32 v74, 0x203, v119
	v_lshl_add_u32 v67, v67, 1, s32
	v_lshl_add_u32 v68, v68, 1, s85
	v_lshl_add_u32 v69, v69, 1, s86
	v_lshl_add_u32 v70, v70, 1, s15
	s_mov_b64 exec, s[70:71]
	ds_write_b16 v67, v71 offset:32768
	s_mov_b64 exec, s[88:89]
	ds_write_b16 v68, v72 offset:32768
	s_mov_b64 exec, s[90:91]
	ds_write_b16 v69, v73 offset:32768
	s_mov_b64 exec, s[94:95]
	ds_write_b16 v70, v74 offset:32768
	s_mov_b64 exec, s[34:35]
	s_mov_b64 s[34:35], exec
	v_cmp_gt_u32_sdwa s[70:71], v40, v66 src0_sel:WORD_0 src1_sel:DWORD
	v_cmp_gt_u32_sdwa s[88:89], v40, v66 src0_sel:WORD_1 src1_sel:DWORD
	v_cmp_gt_u32_sdwa s[90:91], v41, v66 src0_sel:WORD_0 src1_sel:DWORD
	v_cmp_gt_u32_sdwa s[94:95], v41, v66 src0_sel:WORD_1 src1_sel:DWORD
	s_lshl1_add_u32 s32, s4, s52
	v_mbcnt_lo_u32_b32 v67, s70, 0
	v_mbcnt_lo_u32_b32 v68, s88, 0
	v_mbcnt_lo_u32_b32 v69, s90, 0
	v_mbcnt_lo_u32_b32 v70, s94, 0
	s_bcnt1_i32_b64 s93, s[70:71]
	s_add_i32 s4, s4, s93
	s_lshl1_add_u32 s85, s4, s52
	v_mbcnt_hi_u32_b32 v67, s71, v67
	s_bcnt1_i32_b64 s93, s[88:89]
	s_add_i32 s4, s4, s93
	s_lshl1_add_u32 s86, s4, s52
	v_mbcnt_hi_u32_b32 v68, s89, v68
	s_bcnt1_i32_b64 s93, s[90:91]
	s_add_i32 s4, s4, s93
	s_lshl1_add_u32 s15, s4, s52
	v_mbcnt_hi_u32_b32 v69, s91, v69
	s_bcnt1_i32_b64 s93, s[94:95]
	s_add_i32 s4, s4, s93
	v_mbcnt_hi_u32_b32 v70, s95, v70
	v_or_b32_e32 v71, 0x204, v119
	v_or_b32_e32 v72, 0x205, v119
	v_or_b32_e32 v73, 0x206, v119
	v_or_b32_e32 v74, 0x207, v119
	v_lshl_add_u32 v67, v67, 1, s32
	v_lshl_add_u32 v68, v68, 1, s85
	v_lshl_add_u32 v69, v69, 1, s86
	v_lshl_add_u32 v70, v70, 1, s15
	s_mov_b64 exec, s[70:71]
	ds_write_b16 v67, v71 offset:32768
	s_mov_b64 exec, s[88:89]
	ds_write_b16 v68, v72 offset:32768
	s_mov_b64 exec, s[90:91]
	ds_write_b16 v69, v73 offset:32768
	s_mov_b64 exec, s[94:95]
	ds_write_b16 v70, v74 offset:32768
	s_mov_b64 exec, s[34:35]
	s_cmp_gt_i32 s14, 2
	s_cselect_b64 s[74:75], -1, 0
	s_cmp_lt_i32 s14, 3
	s_cbranch_scc1 .LBB0_1279
.LBB0_1309:
	s_mov_b64 s[34:35], exec
	v_cmp_gt_u32_sdwa s[70:71], v26, v66 src0_sel:WORD_0 src1_sel:DWORD
	v_cmp_gt_u32_sdwa s[88:89], v26, v66 src0_sel:WORD_1 src1_sel:DWORD
	v_cmp_gt_u32_sdwa s[90:91], v27, v66 src0_sel:WORD_0 src1_sel:DWORD
	v_cmp_gt_u32_sdwa s[94:95], v27, v66 src0_sel:WORD_1 src1_sel:DWORD
	s_lshl1_add_u32 s32, s4, s52
	v_mbcnt_lo_u32_b32 v67, s70, 0
	v_mbcnt_lo_u32_b32 v68, s88, 0
	v_mbcnt_lo_u32_b32 v69, s90, 0
	v_mbcnt_lo_u32_b32 v70, s94, 0
	s_bcnt1_i32_b64 s93, s[70:71]
	s_add_i32 s4, s4, s93
	s_lshl1_add_u32 s85, s4, s52
	v_mbcnt_hi_u32_b32 v67, s71, v67
	s_bcnt1_i32_b64 s93, s[88:89]
	s_add_i32 s4, s4, s93
	s_lshl1_add_u32 s86, s4, s52
	v_mbcnt_hi_u32_b32 v68, s89, v68
	s_bcnt1_i32_b64 s93, s[90:91]
	s_add_i32 s4, s4, s93
	s_lshl1_add_u32 s15, s4, s52
	v_mbcnt_hi_u32_b32 v69, s91, v69
	s_bcnt1_i32_b64 s93, s[94:95]
	s_add_i32 s4, s4, s93
	v_mbcnt_hi_u32_b32 v70, s95, v70
	v_or_b32_e32 v71, 0x400, v119
	v_or_b32_e32 v72, 0x401, v119
	v_or_b32_e32 v73, 0x402, v119
	v_or_b32_e32 v74, 0x403, v119
	v_lshl_add_u32 v67, v67, 1, s32
	v_lshl_add_u32 v68, v68, 1, s85
	v_lshl_add_u32 v69, v69, 1, s86
	v_lshl_add_u32 v70, v70, 1, s15
	s_mov_b64 exec, s[70:71]
	ds_write_b16 v67, v71 offset:32768
	s_mov_b64 exec, s[88:89]
	ds_write_b16 v68, v72 offset:32768
	s_mov_b64 exec, s[90:91]
	ds_write_b16 v69, v73 offset:32768
	s_mov_b64 exec, s[94:95]
	ds_write_b16 v70, v74 offset:32768
	s_mov_b64 exec, s[34:35]
	s_mov_b64 s[34:35], exec
	v_cmp_gt_u32_sdwa s[70:71], v28, v66 src0_sel:WORD_0 src1_sel:DWORD
	v_cmp_gt_u32_sdwa s[88:89], v28, v66 src0_sel:WORD_1 src1_sel:DWORD
	v_cmp_gt_u32_sdwa s[90:91], v29, v66 src0_sel:WORD_0 src1_sel:DWORD
	v_cmp_gt_u32_sdwa s[94:95], v29, v66 src0_sel:WORD_1 src1_sel:DWORD
	s_lshl1_add_u32 s32, s4, s52
	v_mbcnt_lo_u32_b32 v67, s70, 0
	v_mbcnt_lo_u32_b32 v68, s88, 0
	v_mbcnt_lo_u32_b32 v69, s90, 0
	v_mbcnt_lo_u32_b32 v70, s94, 0
	s_bcnt1_i32_b64 s93, s[70:71]
	s_add_i32 s4, s4, s93
	s_lshl1_add_u32 s85, s4, s52
	v_mbcnt_hi_u32_b32 v67, s71, v67
	s_bcnt1_i32_b64 s93, s[88:89]
	s_add_i32 s4, s4, s93
	s_lshl1_add_u32 s86, s4, s52
	v_mbcnt_hi_u32_b32 v68, s89, v68
	s_bcnt1_i32_b64 s93, s[90:91]
	s_add_i32 s4, s4, s93
	s_lshl1_add_u32 s15, s4, s52
	v_mbcnt_hi_u32_b32 v69, s91, v69
	s_bcnt1_i32_b64 s93, s[94:95]
	s_add_i32 s4, s4, s93
	v_mbcnt_hi_u32_b32 v70, s95, v70
	v_or_b32_e32 v71, 0x404, v119
	v_or_b32_e32 v72, 0x405, v119
	v_or_b32_e32 v73, 0x406, v119
	v_or_b32_e32 v74, 0x407, v119
	v_lshl_add_u32 v67, v67, 1, s32
	v_lshl_add_u32 v68, v68, 1, s85
	v_lshl_add_u32 v69, v69, 1, s86
	v_lshl_add_u32 v70, v70, 1, s15
	s_mov_b64 exec, s[70:71]
	ds_write_b16 v67, v71 offset:32768
	s_mov_b64 exec, s[88:89]
	ds_write_b16 v68, v72 offset:32768
	s_mov_b64 exec, s[90:91]
	ds_write_b16 v69, v73 offset:32768
	s_mov_b64 exec, s[94:95]
	ds_write_b16 v70, v74 offset:32768
	s_mov_b64 exec, s[34:35]
	s_cmp_gt_i32 s14, 3
	s_cselect_b64 s[68:69], -1, 0
	s_cmp_lt_i32 s14, 4
	s_cbranch_scc1 .LBB0_1280
.LBB0_1326:
	s_mov_b64 s[34:35], exec
	v_cmp_gt_u32_sdwa s[70:71], v18, v66 src0_sel:WORD_0 src1_sel:DWORD
	v_cmp_gt_u32_sdwa s[88:89], v18, v66 src0_sel:WORD_1 src1_sel:DWORD
	v_cmp_gt_u32_sdwa s[90:91], v19, v66 src0_sel:WORD_0 src1_sel:DWORD
	v_cmp_gt_u32_sdwa s[94:95], v19, v66 src0_sel:WORD_1 src1_sel:DWORD
	s_lshl1_add_u32 s32, s4, s52
	v_mbcnt_lo_u32_b32 v67, s70, 0
	v_mbcnt_lo_u32_b32 v68, s88, 0
	v_mbcnt_lo_u32_b32 v69, s90, 0
	v_mbcnt_lo_u32_b32 v70, s94, 0
	s_bcnt1_i32_b64 s93, s[70:71]
	s_add_i32 s4, s4, s93
	s_lshl1_add_u32 s85, s4, s52
	v_mbcnt_hi_u32_b32 v67, s71, v67
	s_bcnt1_i32_b64 s93, s[88:89]
	s_add_i32 s4, s4, s93
	s_lshl1_add_u32 s86, s4, s52
	v_mbcnt_hi_u32_b32 v68, s89, v68
	s_bcnt1_i32_b64 s93, s[90:91]
	s_add_i32 s4, s4, s93
	s_lshl1_add_u32 s15, s4, s52
	v_mbcnt_hi_u32_b32 v69, s91, v69
	s_bcnt1_i32_b64 s93, s[94:95]
	s_add_i32 s4, s4, s93
	v_mbcnt_hi_u32_b32 v70, s95, v70
	v_or_b32_e32 v71, 0x600, v119
	v_or_b32_e32 v72, 0x601, v119
	v_or_b32_e32 v73, 0x602, v119
	v_or_b32_e32 v74, 0x603, v119
	v_lshl_add_u32 v67, v67, 1, s32
	v_lshl_add_u32 v68, v68, 1, s85
	v_lshl_add_u32 v69, v69, 1, s86
	v_lshl_add_u32 v70, v70, 1, s15
	s_mov_b64 exec, s[70:71]
	ds_write_b16 v67, v71 offset:32768
	s_mov_b64 exec, s[88:89]
	ds_write_b16 v68, v72 offset:32768
	s_mov_b64 exec, s[90:91]
	ds_write_b16 v69, v73 offset:32768
	s_mov_b64 exec, s[94:95]
	ds_write_b16 v70, v74 offset:32768
	s_mov_b64 exec, s[34:35]
	s_mov_b64 s[34:35], exec
	v_cmp_gt_u32_sdwa s[70:71], v20, v66 src0_sel:WORD_0 src1_sel:DWORD
	v_cmp_gt_u32_sdwa s[88:89], v20, v66 src0_sel:WORD_1 src1_sel:DWORD
	v_cmp_gt_u32_sdwa s[90:91], v21, v66 src0_sel:WORD_0 src1_sel:DWORD
	v_cmp_gt_u32_sdwa s[94:95], v21, v66 src0_sel:WORD_1 src1_sel:DWORD
	s_lshl1_add_u32 s32, s4, s52
	v_mbcnt_lo_u32_b32 v67, s70, 0
	v_mbcnt_lo_u32_b32 v68, s88, 0
	v_mbcnt_lo_u32_b32 v69, s90, 0
	v_mbcnt_lo_u32_b32 v70, s94, 0
	s_bcnt1_i32_b64 s93, s[70:71]
	s_add_i32 s4, s4, s93
	s_lshl1_add_u32 s85, s4, s52
	v_mbcnt_hi_u32_b32 v67, s71, v67
	s_bcnt1_i32_b64 s93, s[88:89]
	s_add_i32 s4, s4, s93
	s_lshl1_add_u32 s86, s4, s52
	v_mbcnt_hi_u32_b32 v68, s89, v68
	s_bcnt1_i32_b64 s93, s[90:91]
	s_add_i32 s4, s4, s93
	s_lshl1_add_u32 s15, s4, s52
	v_mbcnt_hi_u32_b32 v69, s91, v69
	s_bcnt1_i32_b64 s93, s[94:95]
	s_add_i32 s4, s4, s93
	v_mbcnt_hi_u32_b32 v70, s95, v70
	v_or_b32_e32 v71, 0x604, v119
	v_or_b32_e32 v72, 0x605, v119
	v_or_b32_e32 v73, 0x606, v119
	v_or_b32_e32 v74, 0x607, v119
	v_lshl_add_u32 v67, v67, 1, s32
	v_lshl_add_u32 v68, v68, 1, s85
	v_lshl_add_u32 v69, v69, 1, s86
	v_lshl_add_u32 v70, v70, 1, s15
	s_mov_b64 exec, s[70:71]
	ds_write_b16 v67, v71 offset:32768
	s_mov_b64 exec, s[88:89]
	ds_write_b16 v68, v72 offset:32768
	s_mov_b64 exec, s[90:91]
	ds_write_b16 v69, v73 offset:32768
	s_mov_b64 exec, s[94:95]
	ds_write_b16 v70, v74 offset:32768
	s_mov_b64 exec, s[34:35]
	s_and_b64 vcc, exec, s[8:9]
	s_cbranch_vccnz .LBB0_1281
.LBB0_1343:
	s_mov_b64 s[30:31], exec
	v_cmp_gt_u32_sdwa s[70:71], v58, v66 src0_sel:WORD_0 src1_sel:DWORD
	v_cmp_gt_u32_sdwa s[88:89], v58, v66 src0_sel:WORD_1 src1_sel:DWORD
	v_cmp_gt_u32_sdwa s[90:91], v59, v66 src0_sel:WORD_0 src1_sel:DWORD
	v_cmp_gt_u32_sdwa s[94:95], v59, v66 src0_sel:WORD_1 src1_sel:DWORD
	s_lshl1_add_u32 s32, s4, s52
	v_mbcnt_lo_u32_b32 v67, s70, 0
	v_mbcnt_lo_u32_b32 v68, s88, 0
	v_mbcnt_lo_u32_b32 v69, s90, 0
	v_mbcnt_lo_u32_b32 v70, s94, 0
	s_bcnt1_i32_b64 s93, s[70:71]
	s_add_i32 s4, s4, s93
	s_lshl1_add_u32 s85, s4, s52
	v_mbcnt_hi_u32_b32 v67, s71, v67
	s_bcnt1_i32_b64 s93, s[88:89]
	s_add_i32 s4, s4, s93
	s_lshl1_add_u32 s86, s4, s52
	v_mbcnt_hi_u32_b32 v68, s89, v68
	s_bcnt1_i32_b64 s93, s[90:91]
	s_add_i32 s4, s4, s93
	s_lshl1_add_u32 s15, s4, s52
	v_mbcnt_hi_u32_b32 v69, s91, v69
	s_bcnt1_i32_b64 s93, s[94:95]
	s_add_i32 s4, s4, s93
	v_mbcnt_hi_u32_b32 v70, s95, v70
	v_or_b32_e32 v71, 0x800, v119
	v_lshl_add_u32 v67, v67, 1, s32
	v_lshl_add_u32 v68, v68, 1, s85
	v_lshl_add_u32 v69, v69, 1, s86
	v_lshl_add_u32 v70, v70, 1, s15
	s_mov_b64 exec, s[70:71]
	ds_write_b16 v67, v71 offset:32768
	s_mov_b64 exec, s[88:89]
	ds_write_b16 v68, v152 offset:32768
	s_mov_b64 exec, s[90:91]
	ds_write_b16 v69, v153 offset:32768
	s_mov_b64 exec, s[94:95]
	ds_write_b16 v70, v154 offset:32768
	s_mov_b64 exec, s[30:31]
	s_mov_b64 s[30:31], exec
	v_cmp_gt_u32_sdwa s[70:71], v60, v66 src0_sel:WORD_0 src1_sel:DWORD
	v_cmp_gt_u32_sdwa s[88:89], v60, v66 src0_sel:WORD_1 src1_sel:DWORD
	v_cmp_gt_u32_sdwa s[90:91], v61, v66 src0_sel:WORD_0 src1_sel:DWORD
	v_cmp_gt_u32_sdwa s[94:95], v61, v66 src0_sel:WORD_1 src1_sel:DWORD
	s_lshl1_add_u32 s32, s4, s52
	v_mbcnt_lo_u32_b32 v67, s70, 0
	v_mbcnt_lo_u32_b32 v68, s88, 0
	v_mbcnt_lo_u32_b32 v69, s90, 0
	v_mbcnt_lo_u32_b32 v70, s94, 0
	s_bcnt1_i32_b64 s93, s[70:71]
	s_add_i32 s4, s4, s93
	s_lshl1_add_u32 s85, s4, s52
	v_mbcnt_hi_u32_b32 v67, s71, v67
	s_bcnt1_i32_b64 s93, s[88:89]
	s_add_i32 s4, s4, s93
	s_lshl1_add_u32 s86, s4, s52
	v_mbcnt_hi_u32_b32 v68, s89, v68
	s_bcnt1_i32_b64 s93, s[90:91]
	s_add_i32 s4, s4, s93
	s_lshl1_add_u32 s15, s4, s52
	v_mbcnt_hi_u32_b32 v69, s91, v69
	s_bcnt1_i32_b64 s93, s[94:95]
	s_add_i32 s4, s4, s93
	v_mbcnt_hi_u32_b32 v70, s95, v70
	v_lshl_add_u32 v67, v67, 1, s32
	v_lshl_add_u32 v68, v68, 1, s85
	v_lshl_add_u32 v69, v69, 1, s86
	v_lshl_add_u32 v70, v70, 1, s15
	s_mov_b64 exec, s[70:71]
	ds_write_b16 v67, v155 offset:32768
	s_mov_b64 exec, s[88:89]
	ds_write_b16 v68, v156 offset:32768
	s_mov_b64 exec, s[90:91]
	ds_write_b16 v69, v157 offset:32768
	s_mov_b64 exec, s[94:95]
	ds_write_b16 v70, v158 offset:32768
	s_mov_b64 exec, s[30:31]
	s_cmp_gt_i32 s14, 5
	s_cselect_b64 s[66:67], -1, 0
	s_cmp_lt_i32 s14, 6
	s_cbranch_scc1 .LBB0_1282
.LBB0_1360:
	s_mov_b64 s[30:31], exec
	v_cmp_gt_u32_sdwa s[70:71], v46, v66 src0_sel:WORD_0 src1_sel:DWORD
	v_cmp_gt_u32_sdwa s[88:89], v46, v66 src0_sel:WORD_1 src1_sel:DWORD
	v_cmp_gt_u32_sdwa s[90:91], v47, v66 src0_sel:WORD_0 src1_sel:DWORD
	v_cmp_gt_u32_sdwa s[94:95], v47, v66 src0_sel:WORD_1 src1_sel:DWORD
	s_lshl1_add_u32 s32, s4, s52
	v_mbcnt_lo_u32_b32 v67, s70, 0
	v_mbcnt_lo_u32_b32 v68, s88, 0
	v_mbcnt_lo_u32_b32 v69, s90, 0
	v_mbcnt_lo_u32_b32 v70, s94, 0
	s_bcnt1_i32_b64 s93, s[70:71]
	s_add_i32 s4, s4, s93
	s_lshl1_add_u32 s85, s4, s52
	v_mbcnt_hi_u32_b32 v67, s71, v67
	s_bcnt1_i32_b64 s93, s[88:89]
	s_add_i32 s4, s4, s93
	s_lshl1_add_u32 s86, s4, s52
	v_mbcnt_hi_u32_b32 v68, s89, v68
	s_bcnt1_i32_b64 s93, s[90:91]
	s_add_i32 s4, s4, s93
	s_lshl1_add_u32 s15, s4, s52
	v_mbcnt_hi_u32_b32 v69, s91, v69
	s_bcnt1_i32_b64 s93, s[94:95]
	s_add_i32 s4, s4, s93
	v_mbcnt_hi_u32_b32 v70, s95, v70
	v_lshl_add_u32 v67, v67, 1, s32
	v_lshl_add_u32 v68, v68, 1, s85
	v_lshl_add_u32 v69, v69, 1, s86
	v_lshl_add_u32 v70, v70, 1, s15
	s_mov_b64 exec, s[70:71]
	ds_write_b16 v67, v159 offset:32768
	s_mov_b64 exec, s[88:89]
	ds_write_b16 v68, v160 offset:32768
	s_mov_b64 exec, s[90:91]
	ds_write_b16 v69, v161 offset:32768
	s_mov_b64 exec, s[94:95]
	ds_write_b16 v70, v162 offset:32768
	s_mov_b64 exec, s[30:31]
	s_mov_b64 s[30:31], exec
	v_cmp_gt_u32_sdwa s[70:71], v48, v66 src0_sel:WORD_0 src1_sel:DWORD
	v_cmp_gt_u32_sdwa s[88:89], v48, v66 src0_sel:WORD_1 src1_sel:DWORD
	v_cmp_gt_u32_sdwa s[90:91], v49, v66 src0_sel:WORD_0 src1_sel:DWORD
	v_cmp_gt_u32_sdwa s[94:95], v49, v66 src0_sel:WORD_1 src1_sel:DWORD
	s_lshl1_add_u32 s32, s4, s52
	v_mbcnt_lo_u32_b32 v67, s70, 0
	v_mbcnt_lo_u32_b32 v68, s88, 0
	v_mbcnt_lo_u32_b32 v69, s90, 0
	v_mbcnt_lo_u32_b32 v70, s94, 0
	s_bcnt1_i32_b64 s93, s[70:71]
	s_add_i32 s4, s4, s93
	s_lshl1_add_u32 s85, s4, s52
	v_mbcnt_hi_u32_b32 v67, s71, v67
	s_bcnt1_i32_b64 s93, s[88:89]
	s_add_i32 s4, s4, s93
	s_lshl1_add_u32 s86, s4, s52
	v_mbcnt_hi_u32_b32 v68, s89, v68
	s_bcnt1_i32_b64 s93, s[90:91]
	s_add_i32 s4, s4, s93
	s_lshl1_add_u32 s15, s4, s52
	v_mbcnt_hi_u32_b32 v69, s91, v69
	s_bcnt1_i32_b64 s93, s[94:95]
	s_add_i32 s4, s4, s93
	v_mbcnt_hi_u32_b32 v70, s95, v70
	v_lshl_add_u32 v67, v67, 1, s32
	v_lshl_add_u32 v68, v68, 1, s85
	v_lshl_add_u32 v69, v69, 1, s86
	v_lshl_add_u32 v70, v70, 1, s15
	s_mov_b64 exec, s[70:71]
	ds_write_b16 v67, v163 offset:32768
	s_mov_b64 exec, s[88:89]
	ds_write_b16 v68, v164 offset:32768
	s_mov_b64 exec, s[90:91]
	ds_write_b16 v69, v165 offset:32768
	s_mov_b64 exec, s[94:95]
	ds_write_b16 v70, v166 offset:32768
	s_mov_b64 exec, s[30:31]
	s_cmp_gt_i32 s14, 6
	s_cselect_b64 s[64:65], -1, 0
	s_cmp_lt_i32 s14, 7
	s_cbranch_scc1 .LBB0_1283
.LBB0_1377:
	s_mov_b64 s[30:31], exec
	v_cmp_gt_u32_sdwa s[70:71], v34, v66 src0_sel:WORD_0 src1_sel:DWORD
	v_cmp_gt_u32_sdwa s[88:89], v34, v66 src0_sel:WORD_1 src1_sel:DWORD
	v_cmp_gt_u32_sdwa s[90:91], v35, v66 src0_sel:WORD_0 src1_sel:DWORD
	v_cmp_gt_u32_sdwa s[94:95], v35, v66 src0_sel:WORD_1 src1_sel:DWORD
	s_lshl1_add_u32 s32, s4, s52
	v_mbcnt_lo_u32_b32 v67, s70, 0
	v_mbcnt_lo_u32_b32 v68, s88, 0
	v_mbcnt_lo_u32_b32 v69, s90, 0
	v_mbcnt_lo_u32_b32 v70, s94, 0
	s_bcnt1_i32_b64 s93, s[70:71]
	s_add_i32 s4, s4, s93
	s_lshl1_add_u32 s85, s4, s52
	v_mbcnt_hi_u32_b32 v67, s71, v67
	s_bcnt1_i32_b64 s93, s[88:89]
	s_add_i32 s4, s4, s93
	s_lshl1_add_u32 s86, s4, s52
	v_mbcnt_hi_u32_b32 v68, s89, v68
	s_bcnt1_i32_b64 s93, s[90:91]
	s_add_i32 s4, s4, s93
	s_lshl1_add_u32 s15, s4, s52
	v_mbcnt_hi_u32_b32 v69, s91, v69
	s_bcnt1_i32_b64 s93, s[94:95]
	s_add_i32 s4, s4, s93
	v_mbcnt_hi_u32_b32 v70, s95, v70
	v_lshl_add_u32 v67, v67, 1, s32
	v_lshl_add_u32 v68, v68, 1, s85
	v_lshl_add_u32 v69, v69, 1, s86
	v_lshl_add_u32 v70, v70, 1, s15
	s_mov_b64 exec, s[70:71]
	ds_write_b16 v67, v167 offset:32768
	s_mov_b64 exec, s[88:89]
	ds_write_b16 v68, v168 offset:32768
	s_mov_b64 exec, s[90:91]
	ds_write_b16 v69, v169 offset:32768
	s_mov_b64 exec, s[94:95]
	ds_write_b16 v70, v170 offset:32768
	s_mov_b64 exec, s[30:31]
	s_mov_b64 s[30:31], exec
	v_cmp_gt_u32_sdwa s[70:71], v36, v66 src0_sel:WORD_0 src1_sel:DWORD
	v_cmp_gt_u32_sdwa s[88:89], v36, v66 src0_sel:WORD_1 src1_sel:DWORD
	v_cmp_gt_u32_sdwa s[90:91], v37, v66 src0_sel:WORD_0 src1_sel:DWORD
	v_cmp_gt_u32_sdwa s[94:95], v37, v66 src0_sel:WORD_1 src1_sel:DWORD
	s_lshl1_add_u32 s32, s4, s52
	v_mbcnt_lo_u32_b32 v67, s70, 0
	v_mbcnt_lo_u32_b32 v68, s88, 0
	v_mbcnt_lo_u32_b32 v69, s90, 0
	v_mbcnt_lo_u32_b32 v70, s94, 0
	s_bcnt1_i32_b64 s93, s[70:71]
	s_add_i32 s4, s4, s93
	s_lshl1_add_u32 s85, s4, s52
	v_mbcnt_hi_u32_b32 v67, s71, v67
	s_bcnt1_i32_b64 s93, s[88:89]
	s_add_i32 s4, s4, s93
	s_lshl1_add_u32 s86, s4, s52
	v_mbcnt_hi_u32_b32 v68, s89, v68
	s_bcnt1_i32_b64 s93, s[90:91]
	s_add_i32 s4, s4, s93
	s_lshl1_add_u32 s15, s4, s52
	v_mbcnt_hi_u32_b32 v69, s91, v69
	s_bcnt1_i32_b64 s93, s[94:95]
	s_add_i32 s4, s4, s93
	v_mbcnt_hi_u32_b32 v70, s95, v70
	v_lshl_add_u32 v67, v67, 1, s32
	v_lshl_add_u32 v68, v68, 1, s85
	v_lshl_add_u32 v69, v69, 1, s86
	v_lshl_add_u32 v70, v70, 1, s15
	s_mov_b64 exec, s[70:71]
	ds_write_b16 v67, v171 offset:32768
	s_mov_b64 exec, s[88:89]
	ds_write_b16 v68, v172 offset:32768
	s_mov_b64 exec, s[90:91]
	ds_write_b16 v69, v173 offset:32768
	s_mov_b64 exec, s[94:95]
	ds_write_b16 v70, v174 offset:32768
	s_mov_b64 exec, s[30:31]
	s_cmp_gt_i32 s14, 7
	s_cselect_b64 s[58:59], -1, 0
	s_cmp_lt_i32 s14, 8
	s_cbranch_scc1 .LBB0_1284
.LBB0_1394:
	s_mov_b64 s[30:31], exec
	v_cmp_gt_u32_sdwa s[70:71], v22, v66 src0_sel:WORD_0 src1_sel:DWORD
	v_cmp_gt_u32_sdwa s[88:89], v22, v66 src0_sel:WORD_1 src1_sel:DWORD
	v_cmp_gt_u32_sdwa s[90:91], v23, v66 src0_sel:WORD_0 src1_sel:DWORD
	v_cmp_gt_u32_sdwa s[94:95], v23, v66 src0_sel:WORD_1 src1_sel:DWORD
	s_lshl1_add_u32 s32, s4, s52
	v_mbcnt_lo_u32_b32 v67, s70, 0
	v_mbcnt_lo_u32_b32 v68, s88, 0
	v_mbcnt_lo_u32_b32 v69, s90, 0
	v_mbcnt_lo_u32_b32 v70, s94, 0
	s_bcnt1_i32_b64 s93, s[70:71]
	s_add_i32 s4, s4, s93
	s_lshl1_add_u32 s85, s4, s52
	v_mbcnt_hi_u32_b32 v67, s71, v67
	s_bcnt1_i32_b64 s93, s[88:89]
	s_add_i32 s4, s4, s93
	s_lshl1_add_u32 s86, s4, s52
	v_mbcnt_hi_u32_b32 v68, s89, v68
	s_bcnt1_i32_b64 s93, s[90:91]
	s_add_i32 s4, s4, s93
	s_lshl1_add_u32 s15, s4, s52
	v_mbcnt_hi_u32_b32 v69, s91, v69
	s_bcnt1_i32_b64 s93, s[94:95]
	s_add_i32 s4, s4, s93
	v_mbcnt_hi_u32_b32 v70, s95, v70
	v_lshl_add_u32 v67, v67, 1, s32
	v_lshl_add_u32 v68, v68, 1, s85
	v_lshl_add_u32 v69, v69, 1, s86
	v_lshl_add_u32 v70, v70, 1, s15
	s_mov_b64 exec, s[70:71]
	ds_write_b16 v67, v175 offset:32768
	s_mov_b64 exec, s[88:89]
	ds_write_b16 v68, v176 offset:32768
	s_mov_b64 exec, s[90:91]
	ds_write_b16 v69, v177 offset:32768
	s_mov_b64 exec, s[94:95]
	ds_write_b16 v70, v178 offset:32768
	s_mov_b64 exec, s[30:31]
	s_mov_b64 s[30:31], exec
	v_cmp_gt_u32_sdwa s[70:71], v24, v66 src0_sel:WORD_0 src1_sel:DWORD
	v_cmp_gt_u32_sdwa s[88:89], v24, v66 src0_sel:WORD_1 src1_sel:DWORD
	v_cmp_gt_u32_sdwa s[90:91], v25, v66 src0_sel:WORD_0 src1_sel:DWORD
	v_cmp_gt_u32_sdwa s[94:95], v25, v66 src0_sel:WORD_1 src1_sel:DWORD
	s_lshl1_add_u32 s32, s4, s52
	v_mbcnt_lo_u32_b32 v67, s70, 0
	v_mbcnt_lo_u32_b32 v68, s88, 0
	v_mbcnt_lo_u32_b32 v69, s90, 0
	v_mbcnt_lo_u32_b32 v70, s94, 0
	s_bcnt1_i32_b64 s93, s[70:71]
	s_add_i32 s4, s4, s93
	s_lshl1_add_u32 s85, s4, s52
	v_mbcnt_hi_u32_b32 v67, s71, v67
	s_bcnt1_i32_b64 s93, s[88:89]
	s_add_i32 s4, s4, s93
	s_lshl1_add_u32 s86, s4, s52
	v_mbcnt_hi_u32_b32 v68, s89, v68
	s_bcnt1_i32_b64 s93, s[90:91]
	s_add_i32 s4, s4, s93
	s_lshl1_add_u32 s15, s4, s52
	v_mbcnt_hi_u32_b32 v69, s91, v69
	s_bcnt1_i32_b64 s93, s[94:95]
	s_add_i32 s4, s4, s93
	v_mbcnt_hi_u32_b32 v70, s95, v70
	v_lshl_add_u32 v67, v67, 1, s32
	v_lshl_add_u32 v68, v68, 1, s85
	v_lshl_add_u32 v69, v69, 1, s86
	v_lshl_add_u32 v70, v70, 1, s15
	s_mov_b64 exec, s[70:71]
	ds_write_b16 v67, v179 offset:32768
	s_mov_b64 exec, s[88:89]
	ds_write_b16 v68, v180 offset:32768
	s_mov_b64 exec, s[90:91]
	ds_write_b16 v69, v181 offset:32768
	s_mov_b64 exec, s[94:95]
	ds_write_b16 v70, v182 offset:32768
	s_mov_b64 exec, s[30:31]
	s_andn2_b64 vcc, exec, s[26:27]
	s_cbranch_vccnz .LBB0_1285
.LBB0_1411:
	s_mov_b64 s[30:31], exec
	v_cmp_gt_u32_sdwa s[70:71], v62, v66 src0_sel:WORD_0 src1_sel:DWORD
	v_cmp_gt_u32_sdwa s[88:89], v62, v66 src0_sel:WORD_1 src1_sel:DWORD
	v_cmp_gt_u32_sdwa s[90:91], v63, v66 src0_sel:WORD_0 src1_sel:DWORD
	v_cmp_gt_u32_sdwa s[94:95], v63, v66 src0_sel:WORD_1 src1_sel:DWORD
	s_lshl1_add_u32 s32, s4, s52
	v_mbcnt_lo_u32_b32 v67, s70, 0
	v_mbcnt_lo_u32_b32 v68, s88, 0
	v_mbcnt_lo_u32_b32 v69, s90, 0
	v_mbcnt_lo_u32_b32 v70, s94, 0
	s_bcnt1_i32_b64 s93, s[70:71]
	s_add_i32 s4, s4, s93
	s_lshl1_add_u32 s85, s4, s52
	v_mbcnt_hi_u32_b32 v67, s71, v67
	s_bcnt1_i32_b64 s93, s[88:89]
	s_add_i32 s4, s4, s93
	s_lshl1_add_u32 s86, s4, s52
	v_mbcnt_hi_u32_b32 v68, s89, v68
	s_bcnt1_i32_b64 s93, s[90:91]
	s_add_i32 s4, s4, s93
	s_lshl1_add_u32 s15, s4, s52
	v_mbcnt_hi_u32_b32 v69, s91, v69
	s_bcnt1_i32_b64 s93, s[94:95]
	s_add_i32 s4, s4, s93
	v_mbcnt_hi_u32_b32 v70, s95, v70
	v_lshl_add_u32 v67, v67, 1, s32
	v_lshl_add_u32 v68, v68, 1, s85
	v_lshl_add_u32 v69, v69, 1, s86
	v_lshl_add_u32 v70, v70, 1, s15
	s_mov_b64 exec, s[70:71]
	ds_write_b16 v67, v183 offset:32768
	s_mov_b64 exec, s[88:89]
	ds_write_b16 v68, v184 offset:32768
	s_mov_b64 exec, s[90:91]
	ds_write_b16 v69, v185 offset:32768
	s_mov_b64 exec, s[94:95]
	ds_write_b16 v70, v186 offset:32768
	s_mov_b64 exec, s[30:31]
	s_mov_b64 s[30:31], exec
	v_cmp_gt_u32_sdwa s[70:71], v64, v66 src0_sel:WORD_0 src1_sel:DWORD
	v_cmp_gt_u32_sdwa s[88:89], v64, v66 src0_sel:WORD_1 src1_sel:DWORD
	v_cmp_gt_u32_sdwa s[90:91], v65, v66 src0_sel:WORD_0 src1_sel:DWORD
	v_cmp_gt_u32_sdwa s[94:95], v65, v66 src0_sel:WORD_1 src1_sel:DWORD
	s_lshl1_add_u32 s32, s4, s52
	v_mbcnt_lo_u32_b32 v67, s70, 0
	v_mbcnt_lo_u32_b32 v68, s88, 0
	v_mbcnt_lo_u32_b32 v69, s90, 0
	v_mbcnt_lo_u32_b32 v70, s94, 0
	s_bcnt1_i32_b64 s93, s[70:71]
	s_add_i32 s4, s4, s93
	s_lshl1_add_u32 s85, s4, s52
	v_mbcnt_hi_u32_b32 v67, s71, v67
	s_bcnt1_i32_b64 s93, s[88:89]
	s_add_i32 s4, s4, s93
	s_lshl1_add_u32 s86, s4, s52
	v_mbcnt_hi_u32_b32 v68, s89, v68
	s_bcnt1_i32_b64 s93, s[90:91]
	s_add_i32 s4, s4, s93
	s_lshl1_add_u32 s15, s4, s52
	v_mbcnt_hi_u32_b32 v69, s91, v69
	s_bcnt1_i32_b64 s93, s[94:95]
	s_add_i32 s4, s4, s93
	v_mbcnt_hi_u32_b32 v70, s95, v70
	v_lshl_add_u32 v67, v67, 1, s32
	v_lshl_add_u32 v68, v68, 1, s85
	v_lshl_add_u32 v69, v69, 1, s86
	v_lshl_add_u32 v70, v70, 1, s15
	s_mov_b64 exec, s[70:71]
	ds_write_b16 v67, v187 offset:32768
	s_mov_b64 exec, s[88:89]
	ds_write_b16 v68, v188 offset:32768
	s_mov_b64 exec, s[90:91]
	ds_write_b16 v69, v189 offset:32768
	s_mov_b64 exec, s[94:95]
	ds_write_b16 v70, v190 offset:32768
	s_mov_b64 exec, s[30:31]
	s_cmp_gt_i32 s14, 9
	s_cselect_b64 s[44:45], -1, 0
	s_cmp_lt_i32 s14, 10
	s_cbranch_scc1 .LBB0_1286
.LBB0_1428:
	s_mov_b64 s[30:31], exec
	v_cmp_gt_u32_sdwa s[70:71], v54, v66 src0_sel:WORD_0 src1_sel:DWORD
	v_cmp_gt_u32_sdwa s[88:89], v54, v66 src0_sel:WORD_1 src1_sel:DWORD
	v_cmp_gt_u32_sdwa s[90:91], v55, v66 src0_sel:WORD_0 src1_sel:DWORD
	v_cmp_gt_u32_sdwa s[94:95], v55, v66 src0_sel:WORD_1 src1_sel:DWORD
	s_lshl1_add_u32 s32, s4, s52
	v_mbcnt_lo_u32_b32 v67, s70, 0
	v_mbcnt_lo_u32_b32 v68, s88, 0
	v_mbcnt_lo_u32_b32 v69, s90, 0
	v_mbcnt_lo_u32_b32 v70, s94, 0
	s_bcnt1_i32_b64 s93, s[70:71]
	s_add_i32 s4, s4, s93
	s_lshl1_add_u32 s85, s4, s52
	v_mbcnt_hi_u32_b32 v67, s71, v67
	s_bcnt1_i32_b64 s93, s[88:89]
	s_add_i32 s4, s4, s93
	s_lshl1_add_u32 s86, s4, s52
	v_mbcnt_hi_u32_b32 v68, s89, v68
	s_bcnt1_i32_b64 s93, s[90:91]
	s_add_i32 s4, s4, s93
	s_lshl1_add_u32 s15, s4, s52
	v_mbcnt_hi_u32_b32 v69, s91, v69
	s_bcnt1_i32_b64 s93, s[94:95]
	s_add_i32 s4, s4, s93
	v_mbcnt_hi_u32_b32 v70, s95, v70
	v_lshl_add_u32 v67, v67, 1, s32
	v_lshl_add_u32 v68, v68, 1, s85
	v_lshl_add_u32 v69, v69, 1, s86
	v_lshl_add_u32 v70, v70, 1, s15
	s_mov_b64 exec, s[70:71]
	ds_write_b16 v67, v191 offset:32768
	s_mov_b64 exec, s[88:89]
	ds_write_b16 v68, v192 offset:32768
	s_mov_b64 exec, s[90:91]
	ds_write_b16 v69, v193 offset:32768
	s_mov_b64 exec, s[94:95]
	ds_write_b16 v70, v194 offset:32768
	s_mov_b64 exec, s[30:31]
	s_mov_b64 s[30:31], exec
	v_cmp_gt_u32_sdwa s[70:71], v56, v66 src0_sel:WORD_0 src1_sel:DWORD
	v_cmp_gt_u32_sdwa s[88:89], v56, v66 src0_sel:WORD_1 src1_sel:DWORD
	v_cmp_gt_u32_sdwa s[90:91], v57, v66 src0_sel:WORD_0 src1_sel:DWORD
	v_cmp_gt_u32_sdwa s[94:95], v57, v66 src0_sel:WORD_1 src1_sel:DWORD
	s_lshl1_add_u32 s32, s4, s52
	v_mbcnt_lo_u32_b32 v67, s70, 0
	v_mbcnt_lo_u32_b32 v68, s88, 0
	v_mbcnt_lo_u32_b32 v69, s90, 0
	v_mbcnt_lo_u32_b32 v70, s94, 0
	s_bcnt1_i32_b64 s93, s[70:71]
	s_add_i32 s4, s4, s93
	s_lshl1_add_u32 s85, s4, s52
	v_mbcnt_hi_u32_b32 v67, s71, v67
	s_bcnt1_i32_b64 s93, s[88:89]
	s_add_i32 s4, s4, s93
	s_lshl1_add_u32 s86, s4, s52
	v_mbcnt_hi_u32_b32 v68, s89, v68
	s_bcnt1_i32_b64 s93, s[90:91]
	s_add_i32 s4, s4, s93
	s_lshl1_add_u32 s15, s4, s52
	v_mbcnt_hi_u32_b32 v69, s91, v69
	s_bcnt1_i32_b64 s93, s[94:95]
	s_add_i32 s4, s4, s93
	v_mbcnt_hi_u32_b32 v70, s95, v70
	v_lshl_add_u32 v67, v67, 1, s32
	v_lshl_add_u32 v68, v68, 1, s85
	v_lshl_add_u32 v69, v69, 1, s86
	v_lshl_add_u32 v70, v70, 1, s15
	s_mov_b64 exec, s[70:71]
	ds_write_b16 v67, v195 offset:32768
	s_mov_b64 exec, s[88:89]
	ds_write_b16 v68, v196 offset:32768
	s_mov_b64 exec, s[90:91]
	ds_write_b16 v69, v197 offset:32768
	s_mov_b64 exec, s[94:95]
	ds_write_b16 v70, v198 offset:32768
	s_mov_b64 exec, s[30:31]
	s_cmp_gt_i32 s14, 10
	s_cselect_b64 s[40:41], -1, 0
	s_cmp_lt_i32 s14, 11
	s_cbranch_scc1 .LBB0_1287
.LBB0_1445:
	s_mov_b64 s[30:31], exec
	v_cmp_gt_u32_sdwa s[70:71], v42, v66 src0_sel:WORD_0 src1_sel:DWORD
	v_cmp_gt_u32_sdwa s[88:89], v42, v66 src0_sel:WORD_1 src1_sel:DWORD
	v_cmp_gt_u32_sdwa s[90:91], v43, v66 src0_sel:WORD_0 src1_sel:DWORD
	v_cmp_gt_u32_sdwa s[94:95], v43, v66 src0_sel:WORD_1 src1_sel:DWORD
	s_lshl1_add_u32 s32, s4, s52
	v_mbcnt_lo_u32_b32 v67, s70, 0
	v_mbcnt_lo_u32_b32 v68, s88, 0
	v_mbcnt_lo_u32_b32 v69, s90, 0
	v_mbcnt_lo_u32_b32 v70, s94, 0
	s_bcnt1_i32_b64 s93, s[70:71]
	s_add_i32 s4, s4, s93
	s_lshl1_add_u32 s85, s4, s52
	v_mbcnt_hi_u32_b32 v67, s71, v67
	s_bcnt1_i32_b64 s93, s[88:89]
	s_add_i32 s4, s4, s93
	s_lshl1_add_u32 s86, s4, s52
	v_mbcnt_hi_u32_b32 v68, s89, v68
	s_bcnt1_i32_b64 s93, s[90:91]
	s_add_i32 s4, s4, s93
	s_lshl1_add_u32 s15, s4, s52
	v_mbcnt_hi_u32_b32 v69, s91, v69
	s_bcnt1_i32_b64 s93, s[94:95]
	s_add_i32 s4, s4, s93
	v_mbcnt_hi_u32_b32 v70, s95, v70
	v_lshl_add_u32 v67, v67, 1, s32
	v_lshl_add_u32 v68, v68, 1, s85
	v_lshl_add_u32 v69, v69, 1, s86
	v_lshl_add_u32 v70, v70, 1, s15
	s_mov_b64 exec, s[70:71]
	ds_write_b16 v67, v199 offset:32768
	s_mov_b64 exec, s[88:89]
	ds_write_b16 v68, v200 offset:32768
	s_mov_b64 exec, s[90:91]
	ds_write_b16 v69, v201 offset:32768
	s_mov_b64 exec, s[94:95]
	ds_write_b16 v70, v202 offset:32768
	s_mov_b64 exec, s[30:31]
	s_mov_b64 s[30:31], exec
	v_cmp_gt_u32_sdwa s[70:71], v44, v66 src0_sel:WORD_0 src1_sel:DWORD
	v_cmp_gt_u32_sdwa s[88:89], v44, v66 src0_sel:WORD_1 src1_sel:DWORD
	v_cmp_gt_u32_sdwa s[90:91], v45, v66 src0_sel:WORD_0 src1_sel:DWORD
	v_cmp_gt_u32_sdwa s[94:95], v45, v66 src0_sel:WORD_1 src1_sel:DWORD
	s_lshl1_add_u32 s32, s4, s52
	v_mbcnt_lo_u32_b32 v67, s70, 0
	v_mbcnt_lo_u32_b32 v68, s88, 0
	v_mbcnt_lo_u32_b32 v69, s90, 0
	v_mbcnt_lo_u32_b32 v70, s94, 0
	s_bcnt1_i32_b64 s93, s[70:71]
	s_add_i32 s4, s4, s93
	s_lshl1_add_u32 s85, s4, s52
	v_mbcnt_hi_u32_b32 v67, s71, v67
	s_bcnt1_i32_b64 s93, s[88:89]
	s_add_i32 s4, s4, s93
	s_lshl1_add_u32 s86, s4, s52
	v_mbcnt_hi_u32_b32 v68, s89, v68
	s_bcnt1_i32_b64 s93, s[90:91]
	s_add_i32 s4, s4, s93
	s_lshl1_add_u32 s15, s4, s52
	v_mbcnt_hi_u32_b32 v69, s91, v69
	s_bcnt1_i32_b64 s93, s[94:95]
	s_add_i32 s4, s4, s93
	v_mbcnt_hi_u32_b32 v70, s95, v70
	v_lshl_add_u32 v67, v67, 1, s32
	v_lshl_add_u32 v68, v68, 1, s85
	v_lshl_add_u32 v69, v69, 1, s86
	v_lshl_add_u32 v70, v70, 1, s15
	s_mov_b64 exec, s[70:71]
	ds_write_b16 v67, v203 offset:32768
	s_mov_b64 exec, s[88:89]
	ds_write_b16 v68, v204 offset:32768
	s_mov_b64 exec, s[90:91]
	ds_write_b16 v69, v205 offset:32768
	s_mov_b64 exec, s[94:95]
	ds_write_b16 v70, v206 offset:32768
	s_mov_b64 exec, s[30:31]
	s_cmp_gt_i32 s14, 11
	s_cselect_b64 s[38:39], -1, 0
	s_cmp_lt_i32 s14, 12
	s_cbranch_scc1 .LBB0_1288
.LBB0_1462:
	s_mov_b64 s[30:31], exec
	v_cmp_gt_u32_sdwa s[70:71], v30, v66 src0_sel:WORD_0 src1_sel:DWORD
	v_cmp_gt_u32_sdwa s[88:89], v30, v66 src0_sel:WORD_1 src1_sel:DWORD
	v_cmp_gt_u32_sdwa s[90:91], v31, v66 src0_sel:WORD_0 src1_sel:DWORD
	v_cmp_gt_u32_sdwa s[94:95], v31, v66 src0_sel:WORD_1 src1_sel:DWORD
	s_lshl1_add_u32 s32, s4, s52
	v_mbcnt_lo_u32_b32 v67, s70, 0
	v_mbcnt_lo_u32_b32 v68, s88, 0
	v_mbcnt_lo_u32_b32 v69, s90, 0
	v_mbcnt_lo_u32_b32 v70, s94, 0
	s_bcnt1_i32_b64 s93, s[70:71]
	s_add_i32 s4, s4, s93
	s_lshl1_add_u32 s85, s4, s52
	v_mbcnt_hi_u32_b32 v67, s71, v67
	s_bcnt1_i32_b64 s93, s[88:89]
	s_add_i32 s4, s4, s93
	s_lshl1_add_u32 s86, s4, s52
	v_mbcnt_hi_u32_b32 v68, s89, v68
	s_bcnt1_i32_b64 s93, s[90:91]
	s_add_i32 s4, s4, s93
	s_lshl1_add_u32 s15, s4, s52
	v_mbcnt_hi_u32_b32 v69, s91, v69
	s_bcnt1_i32_b64 s93, s[94:95]
	s_add_i32 s4, s4, s93
	v_mbcnt_hi_u32_b32 v70, s95, v70
	v_lshl_add_u32 v67, v67, 1, s32
	v_lshl_add_u32 v68, v68, 1, s85
	v_lshl_add_u32 v69, v69, 1, s86
	v_lshl_add_u32 v70, v70, 1, s15
	s_mov_b64 exec, s[70:71]
	ds_write_b16 v67, v207 offset:32768
	s_mov_b64 exec, s[88:89]
	ds_write_b16 v68, v208 offset:32768
	s_mov_b64 exec, s[90:91]
	ds_write_b16 v69, v209 offset:32768
	s_mov_b64 exec, s[94:95]
	ds_write_b16 v70, v210 offset:32768
	s_mov_b64 exec, s[30:31]
	s_mov_b64 s[30:31], exec
	v_cmp_gt_u32_sdwa s[70:71], v32, v66 src0_sel:WORD_0 src1_sel:DWORD
	v_cmp_gt_u32_sdwa s[88:89], v32, v66 src0_sel:WORD_1 src1_sel:DWORD
	v_cmp_gt_u32_sdwa s[90:91], v33, v66 src0_sel:WORD_0 src1_sel:DWORD
	v_cmp_gt_u32_sdwa s[94:95], v33, v66 src0_sel:WORD_1 src1_sel:DWORD
	s_lshl1_add_u32 s32, s4, s52
	v_mbcnt_lo_u32_b32 v67, s70, 0
	v_mbcnt_lo_u32_b32 v68, s88, 0
	v_mbcnt_lo_u32_b32 v69, s90, 0
	v_mbcnt_lo_u32_b32 v70, s94, 0
	s_bcnt1_i32_b64 s93, s[70:71]
	s_add_i32 s4, s4, s93
	s_lshl1_add_u32 s85, s4, s52
	v_mbcnt_hi_u32_b32 v67, s71, v67
	s_bcnt1_i32_b64 s93, s[88:89]
	s_add_i32 s4, s4, s93
	s_lshl1_add_u32 s86, s4, s52
	v_mbcnt_hi_u32_b32 v68, s89, v68
	s_bcnt1_i32_b64 s93, s[90:91]
	s_add_i32 s4, s4, s93
	s_lshl1_add_u32 s15, s4, s52
	v_mbcnt_hi_u32_b32 v69, s91, v69
	s_bcnt1_i32_b64 s93, s[94:95]
	s_add_i32 s4, s4, s93
	v_mbcnt_hi_u32_b32 v70, s95, v70
	v_lshl_add_u32 v67, v67, 1, s32
	v_lshl_add_u32 v68, v68, 1, s85
	v_lshl_add_u32 v69, v69, 1, s86
	v_lshl_add_u32 v70, v70, 1, s15
	s_mov_b64 exec, s[70:71]
	ds_write_b16 v67, v211 offset:32768
	s_mov_b64 exec, s[88:89]
	ds_write_b16 v68, v212 offset:32768
	s_mov_b64 exec, s[90:91]
	ds_write_b16 v69, v213 offset:32768
	s_mov_b64 exec, s[94:95]
	ds_write_b16 v70, v214 offset:32768
	s_mov_b64 exec, s[30:31]
	s_andn2_b64 vcc, exec, s[2:3]
	s_cbranch_vccnz .LBB0_1289
.LBB0_1479:
	s_mov_b64 s[30:31], exec
	v_cmp_gt_u32_sdwa s[70:71], v14, v66 src0_sel:WORD_0 src1_sel:DWORD
	v_cmp_gt_u32_sdwa s[88:89], v14, v66 src0_sel:WORD_1 src1_sel:DWORD
	v_cmp_gt_u32_sdwa s[90:91], v15, v66 src0_sel:WORD_0 src1_sel:DWORD
	v_cmp_gt_u32_sdwa s[94:95], v15, v66 src0_sel:WORD_1 src1_sel:DWORD
	s_lshl1_add_u32 s32, s4, s52
	v_mbcnt_lo_u32_b32 v67, s70, 0
	v_mbcnt_lo_u32_b32 v68, s88, 0
	v_mbcnt_lo_u32_b32 v69, s90, 0
	v_mbcnt_lo_u32_b32 v70, s94, 0
	s_bcnt1_i32_b64 s93, s[70:71]
	s_add_i32 s4, s4, s93
	s_lshl1_add_u32 s85, s4, s52
	v_mbcnt_hi_u32_b32 v67, s71, v67
	s_bcnt1_i32_b64 s93, s[88:89]
	s_add_i32 s4, s4, s93
	s_lshl1_add_u32 s86, s4, s52
	v_mbcnt_hi_u32_b32 v68, s89, v68
	s_bcnt1_i32_b64 s93, s[90:91]
	s_add_i32 s4, s4, s93
	s_lshl1_add_u32 s15, s4, s52
	v_mbcnt_hi_u32_b32 v69, s91, v69
	s_bcnt1_i32_b64 s93, s[94:95]
	s_add_i32 s4, s4, s93
	v_mbcnt_hi_u32_b32 v70, s95, v70
	v_lshl_add_u32 v67, v67, 1, s32
	v_lshl_add_u32 v68, v68, 1, s85
	v_lshl_add_u32 v69, v69, 1, s86
	v_lshl_add_u32 v70, v70, 1, s15
	s_mov_b64 exec, s[70:71]
	ds_write_b16 v67, v215 offset:32768
	s_mov_b64 exec, s[88:89]
	ds_write_b16 v68, v216 offset:32768
	s_mov_b64 exec, s[90:91]
	ds_write_b16 v69, v217 offset:32768
	s_mov_b64 exec, s[94:95]
	ds_write_b16 v70, v218 offset:32768
	s_mov_b64 exec, s[30:31]
	s_mov_b64 s[30:31], exec
	v_cmp_gt_u32_sdwa s[70:71], v16, v66 src0_sel:WORD_0 src1_sel:DWORD
	v_cmp_gt_u32_sdwa s[88:89], v16, v66 src0_sel:WORD_1 src1_sel:DWORD
	v_cmp_gt_u32_sdwa s[90:91], v17, v66 src0_sel:WORD_0 src1_sel:DWORD
	v_cmp_gt_u32_sdwa s[94:95], v17, v66 src0_sel:WORD_1 src1_sel:DWORD
	s_lshl1_add_u32 s32, s4, s52
	v_mbcnt_lo_u32_b32 v67, s70, 0
	v_mbcnt_lo_u32_b32 v68, s88, 0
	v_mbcnt_lo_u32_b32 v69, s90, 0
	v_mbcnt_lo_u32_b32 v70, s94, 0
	s_bcnt1_i32_b64 s93, s[70:71]
	s_add_i32 s4, s4, s93
	s_lshl1_add_u32 s85, s4, s52
	v_mbcnt_hi_u32_b32 v67, s71, v67
	s_bcnt1_i32_b64 s93, s[88:89]
	s_add_i32 s4, s4, s93
	s_lshl1_add_u32 s86, s4, s52
	v_mbcnt_hi_u32_b32 v68, s89, v68
	s_bcnt1_i32_b64 s93, s[90:91]
	s_add_i32 s4, s4, s93
	s_lshl1_add_u32 s15, s4, s52
	v_mbcnt_hi_u32_b32 v69, s91, v69
	s_bcnt1_i32_b64 s93, s[94:95]
	s_add_i32 s4, s4, s93
	v_mbcnt_hi_u32_b32 v70, s95, v70
	v_lshl_add_u32 v67, v67, 1, s32
	v_lshl_add_u32 v68, v68, 1, s85
	v_lshl_add_u32 v69, v69, 1, s86
	v_lshl_add_u32 v70, v70, 1, s15
	s_mov_b64 exec, s[70:71]
	ds_write_b16 v67, v219 offset:32768
	s_mov_b64 exec, s[88:89]
	ds_write_b16 v68, v220 offset:32768
	s_mov_b64 exec, s[90:91]
	ds_write_b16 v69, v221 offset:32768
	s_mov_b64 exec, s[94:95]
	ds_write_b16 v70, v222 offset:32768
	s_mov_b64 exec, s[30:31]
	s_cmp_gt_i32 s14, 13
	s_cselect_b64 s[36:37], -1, 0
	s_cmp_lt_i32 s14, 14
	s_cbranch_scc1 .LBB0_1290
.LBB0_1496:
	s_mov_b64 s[30:31], exec
	v_cmp_gt_u32_sdwa s[70:71], v10, v66 src0_sel:WORD_0 src1_sel:DWORD
	v_cmp_gt_u32_sdwa s[88:89], v10, v66 src0_sel:WORD_1 src1_sel:DWORD
	v_cmp_gt_u32_sdwa s[90:91], v11, v66 src0_sel:WORD_0 src1_sel:DWORD
	v_cmp_gt_u32_sdwa s[94:95], v11, v66 src0_sel:WORD_1 src1_sel:DWORD
	s_lshl1_add_u32 s32, s4, s52
	v_mbcnt_lo_u32_b32 v67, s70, 0
	v_mbcnt_lo_u32_b32 v68, s88, 0
	v_mbcnt_lo_u32_b32 v69, s90, 0
	v_mbcnt_lo_u32_b32 v70, s94, 0
	s_bcnt1_i32_b64 s93, s[70:71]
	s_add_i32 s4, s4, s93
	s_lshl1_add_u32 s85, s4, s52
	v_mbcnt_hi_u32_b32 v67, s71, v67
	s_bcnt1_i32_b64 s93, s[88:89]
	s_add_i32 s4, s4, s93
	s_lshl1_add_u32 s86, s4, s52
	v_mbcnt_hi_u32_b32 v68, s89, v68
	s_bcnt1_i32_b64 s93, s[90:91]
	s_add_i32 s4, s4, s93
	s_lshl1_add_u32 s15, s4, s52
	v_mbcnt_hi_u32_b32 v69, s91, v69
	s_bcnt1_i32_b64 s93, s[94:95]
	s_add_i32 s4, s4, s93
	v_mbcnt_hi_u32_b32 v70, s95, v70
	v_lshl_add_u32 v67, v67, 1, s32
	v_lshl_add_u32 v68, v68, 1, s85
	v_lshl_add_u32 v69, v69, 1, s86
	v_lshl_add_u32 v70, v70, 1, s15
	s_mov_b64 exec, s[70:71]
	ds_write_b16 v67, v223 offset:32768
	s_mov_b64 exec, s[88:89]
	ds_write_b16 v68, v224 offset:32768
	s_mov_b64 exec, s[90:91]
	ds_write_b16 v69, v225 offset:32768
	s_mov_b64 exec, s[94:95]
	ds_write_b16 v70, v226 offset:32768
	s_mov_b64 exec, s[30:31]
	s_mov_b64 s[30:31], exec
	v_cmp_gt_u32_sdwa s[70:71], v12, v66 src0_sel:WORD_0 src1_sel:DWORD
	v_cmp_gt_u32_sdwa s[88:89], v12, v66 src0_sel:WORD_1 src1_sel:DWORD
	v_cmp_gt_u32_sdwa s[90:91], v13, v66 src0_sel:WORD_0 src1_sel:DWORD
	v_cmp_gt_u32_sdwa s[94:95], v13, v66 src0_sel:WORD_1 src1_sel:DWORD
	s_lshl1_add_u32 s32, s4, s52
	v_mbcnt_lo_u32_b32 v67, s70, 0
	v_mbcnt_lo_u32_b32 v68, s88, 0
	v_mbcnt_lo_u32_b32 v69, s90, 0
	v_mbcnt_lo_u32_b32 v70, s94, 0
	s_bcnt1_i32_b64 s93, s[70:71]
	s_add_i32 s4, s4, s93
	s_lshl1_add_u32 s85, s4, s52
	v_mbcnt_hi_u32_b32 v67, s71, v67
	s_bcnt1_i32_b64 s93, s[88:89]
	s_add_i32 s4, s4, s93
	s_lshl1_add_u32 s86, s4, s52
	v_mbcnt_hi_u32_b32 v68, s89, v68
	s_bcnt1_i32_b64 s93, s[90:91]
	s_add_i32 s4, s4, s93
	s_lshl1_add_u32 s15, s4, s52
	v_mbcnt_hi_u32_b32 v69, s91, v69
	s_bcnt1_i32_b64 s93, s[94:95]
	s_add_i32 s4, s4, s93
	v_mbcnt_hi_u32_b32 v70, s95, v70
	v_lshl_add_u32 v67, v67, 1, s32
	v_lshl_add_u32 v68, v68, 1, s85
	v_lshl_add_u32 v69, v69, 1, s86
	v_lshl_add_u32 v70, v70, 1, s15
	s_mov_b64 exec, s[70:71]
	ds_write_b16 v67, v227 offset:32768
	s_mov_b64 exec, s[88:89]
	ds_write_b16 v68, v228 offset:32768
	s_mov_b64 exec, s[90:91]
	ds_write_b16 v69, v229 offset:32768
	s_mov_b64 exec, s[94:95]
	ds_write_b16 v70, v230 offset:32768
	s_mov_b64 exec, s[30:31]
	s_cmp_gt_i32 s14, 14
	s_cselect_b64 s[34:35], -1, 0
	s_cmp_lt_i32 s14, 15
	s_cbranch_scc1 .LBB0_1291
.LBB0_1513:
	s_mov_b64 s[30:31], exec
	v_cmp_gt_u32_sdwa s[70:71], v6, v66 src0_sel:WORD_0 src1_sel:DWORD
	v_cmp_gt_u32_sdwa s[88:89], v6, v66 src0_sel:WORD_1 src1_sel:DWORD
	v_cmp_gt_u32_sdwa s[90:91], v7, v66 src0_sel:WORD_0 src1_sel:DWORD
	v_cmp_gt_u32_sdwa s[94:95], v7, v66 src0_sel:WORD_1 src1_sel:DWORD
	s_lshl1_add_u32 s32, s4, s52
	v_mbcnt_lo_u32_b32 v67, s70, 0
	v_mbcnt_lo_u32_b32 v68, s88, 0
	v_mbcnt_lo_u32_b32 v69, s90, 0
	v_mbcnt_lo_u32_b32 v70, s94, 0
	s_bcnt1_i32_b64 s93, s[70:71]
	s_add_i32 s4, s4, s93
	s_lshl1_add_u32 s85, s4, s52
	v_mbcnt_hi_u32_b32 v67, s71, v67
	s_bcnt1_i32_b64 s93, s[88:89]
	s_add_i32 s4, s4, s93
	s_lshl1_add_u32 s86, s4, s52
	v_mbcnt_hi_u32_b32 v68, s89, v68
	s_bcnt1_i32_b64 s93, s[90:91]
	s_add_i32 s4, s4, s93
	s_lshl1_add_u32 s15, s4, s52
	v_mbcnt_hi_u32_b32 v69, s91, v69
	s_bcnt1_i32_b64 s93, s[94:95]
	s_add_i32 s4, s4, s93
	v_mbcnt_hi_u32_b32 v70, s95, v70
	v_lshl_add_u32 v67, v67, 1, s32
	v_lshl_add_u32 v68, v68, 1, s85
	v_lshl_add_u32 v69, v69, 1, s86
	v_lshl_add_u32 v70, v70, 1, s15
	s_mov_b64 exec, s[70:71]
	ds_write_b16 v67, v231 offset:32768
	s_mov_b64 exec, s[88:89]
	ds_write_b16 v68, v232 offset:32768
	s_mov_b64 exec, s[90:91]
	ds_write_b16 v69, v233 offset:32768
	s_mov_b64 exec, s[94:95]
	ds_write_b16 v70, v234 offset:32768
	s_mov_b64 exec, s[30:31]
	s_mov_b64 s[30:31], exec
	v_cmp_gt_u32_sdwa s[70:71], v8, v66 src0_sel:WORD_0 src1_sel:DWORD
	v_cmp_gt_u32_sdwa s[88:89], v8, v66 src0_sel:WORD_1 src1_sel:DWORD
	v_cmp_gt_u32_sdwa s[90:91], v9, v66 src0_sel:WORD_0 src1_sel:DWORD
	v_cmp_gt_u32_sdwa s[94:95], v9, v66 src0_sel:WORD_1 src1_sel:DWORD
	s_lshl1_add_u32 s32, s4, s52
	v_mbcnt_lo_u32_b32 v67, s70, 0
	v_mbcnt_lo_u32_b32 v68, s88, 0
	v_mbcnt_lo_u32_b32 v69, s90, 0
	v_mbcnt_lo_u32_b32 v70, s94, 0
	s_bcnt1_i32_b64 s93, s[70:71]
	s_add_i32 s4, s4, s93
	s_lshl1_add_u32 s85, s4, s52
	v_mbcnt_hi_u32_b32 v67, s71, v67
	s_bcnt1_i32_b64 s93, s[88:89]
	s_add_i32 s4, s4, s93
	s_lshl1_add_u32 s86, s4, s52
	v_mbcnt_hi_u32_b32 v68, s89, v68
	s_bcnt1_i32_b64 s93, s[90:91]
	s_add_i32 s4, s4, s93
	s_lshl1_add_u32 s15, s4, s52
	v_mbcnt_hi_u32_b32 v69, s91, v69
	s_bcnt1_i32_b64 s93, s[94:95]
	s_add_i32 s4, s4, s93
	v_mbcnt_hi_u32_b32 v70, s95, v70
	v_lshl_add_u32 v67, v67, 1, s32
	v_lshl_add_u32 v68, v68, 1, s85
	v_lshl_add_u32 v69, v69, 1, s86
	v_lshl_add_u32 v70, v70, 1, s15
	s_mov_b64 exec, s[70:71]
	ds_write_b16 v67, v235 offset:32768
	s_mov_b64 exec, s[88:89]
	ds_write_b16 v68, v236 offset:32768
	s_mov_b64 exec, s[90:91]
	ds_write_b16 v69, v237 offset:32768
	s_mov_b64 exec, s[94:95]
	ds_write_b16 v70, v238 offset:32768
	s_mov_b64 exec, s[30:31]
	s_cmp_gt_i32 s14, 15
	s_cselect_b64 s[30:31], -1, 0
	s_cmp_lt_i32 s14, 16
	s_cbranch_scc1 .LBB0_1547
.LBB0_1530:
	s_mov_b64 vcc, exec
	v_cmp_gt_u32_sdwa s[70:71], v2, v66 src0_sel:WORD_0 src1_sel:DWORD
	v_cmp_gt_u32_sdwa s[88:89], v2, v66 src0_sel:WORD_1 src1_sel:DWORD
	v_cmp_gt_u32_sdwa s[90:91], v3, v66 src0_sel:WORD_0 src1_sel:DWORD
	v_cmp_gt_u32_sdwa s[94:95], v3, v66 src0_sel:WORD_1 src1_sel:DWORD
	s_lshl1_add_u32 s32, s4, s52
	v_mbcnt_lo_u32_b32 v67, s70, 0
	v_mbcnt_lo_u32_b32 v68, s88, 0
	v_mbcnt_lo_u32_b32 v69, s90, 0
	v_mbcnt_lo_u32_b32 v70, s94, 0
	s_bcnt1_i32_b64 s93, s[70:71]
	s_add_i32 s4, s4, s93
	s_lshl1_add_u32 s85, s4, s52
	v_mbcnt_hi_u32_b32 v67, s71, v67
	s_bcnt1_i32_b64 s93, s[88:89]
	s_add_i32 s4, s4, s93
	s_lshl1_add_u32 s86, s4, s52
	v_mbcnt_hi_u32_b32 v68, s89, v68
	s_bcnt1_i32_b64 s93, s[90:91]
	s_add_i32 s4, s4, s93
	s_lshl1_add_u32 s14, s4, s52
	v_mbcnt_hi_u32_b32 v69, s91, v69
	s_bcnt1_i32_b64 s93, s[94:95]
	s_add_i32 s4, s4, s93
	v_mbcnt_hi_u32_b32 v70, s95, v70
	v_lshl_add_u32 v67, v67, 1, s32
	v_lshl_add_u32 v68, v68, 1, s85
	v_lshl_add_u32 v69, v69, 1, s86
	v_lshl_add_u32 v70, v70, 1, s14
	s_mov_b64 exec, s[70:71]
	ds_write_b16 v67, v239 offset:32768
	s_mov_b64 exec, s[88:89]
	ds_write_b16 v68, v240 offset:32768
	s_mov_b64 exec, s[90:91]
	ds_write_b16 v69, v241 offset:32768
	s_mov_b64 exec, s[94:95]
	ds_write_b16 v70, v242 offset:32768
	s_mov_b64 exec, vcc
	s_mov_b64 vcc, exec
	v_cmp_gt_u32_sdwa s[70:71], v4, v66 src0_sel:WORD_0 src1_sel:DWORD
	v_cmp_gt_u32_sdwa s[88:89], v4, v66 src0_sel:WORD_1 src1_sel:DWORD
	v_cmp_gt_u32_sdwa s[90:91], v5, v66 src0_sel:WORD_0 src1_sel:DWORD
	v_cmp_gt_u32_sdwa s[94:95], v5, v66 src0_sel:WORD_1 src1_sel:DWORD
	s_lshl1_add_u32 s32, s4, s52
	v_mbcnt_lo_u32_b32 v67, s70, 0
	v_mbcnt_lo_u32_b32 v68, s88, 0
	v_mbcnt_lo_u32_b32 v69, s90, 0
	v_mbcnt_lo_u32_b32 v70, s94, 0
	s_bcnt1_i32_b64 s93, s[70:71]
	s_add_i32 s4, s4, s93
	s_lshl1_add_u32 s85, s4, s52
	v_mbcnt_hi_u32_b32 v67, s71, v67
	s_bcnt1_i32_b64 s93, s[88:89]
	s_add_i32 s4, s4, s93
	s_lshl1_add_u32 s86, s4, s52
	v_mbcnt_hi_u32_b32 v68, s89, v68
	s_bcnt1_i32_b64 s93, s[90:91]
	s_add_i32 s4, s4, s93
	s_lshl1_add_u32 s14, s4, s52
	v_mbcnt_hi_u32_b32 v69, s91, v69
	s_bcnt1_i32_b64 s93, s[94:95]
	s_add_i32 s4, s4, s93
	v_mbcnt_hi_u32_b32 v70, s95, v70
	v_lshl_add_u32 v67, v67, 1, s32
	v_lshl_add_u32 v68, v68, 1, s85
	v_lshl_add_u32 v69, v69, 1, s86
	v_lshl_add_u32 v70, v70, 1, s14
	s_mov_b64 exec, s[70:71]
	ds_write_b16 v67, v243 offset:32768
	s_mov_b64 exec, s[88:89]
	ds_write_b16 v68, v244 offset:32768
	s_mov_b64 exec, s[90:91]
	ds_write_b16 v69, v245 offset:32768
	s_mov_b64 exec, s[94:95]
	ds_write_b16 v70, v246 offset:32768
	s_mov_b64 exec, vcc
